# v60 + P3 MoE weight conversion loop rewritten: single path with SGPR-base addressing, next item's loads issued before the current item's LDS transpose (software pipelined)
# baseline (speedup 1.0000x reference)
.LBB0_357:
	s_waitcnt lgkmcnt(0)
	v_mov_b32_e32 v0, v189
	s_nop 1
	v_permlane32_swap_b32_e32 v189, v0
	s_and_saveexec_b64 s[0:1], s[4:5]
	v_add_f32_e32 v0, v189, v0
	ds_write_b32 v179, v0 offset:128
	s_or_b64 exec, exec, s[0:1]
	s_waitcnt lgkmcnt(0)
	v_add_u32_e32 v0, s25, v180
	ds_read_b128 v[34:37], v0 offset:128
	ds_read_b128 v[38:41], v0 offset:160
	s_or_b32 s0, s75, s77
	s_or_b32 s0, s0, s74
	s_mulk_i32 s0, 0x600
	s_waitcnt lgkmcnt(0)
	v_rcp_f32_e32 v42, v34
	v_rcp_f32_e32 v43, v35
	v_rcp_f32_e32 v44, v36
	v_rcp_f32_e32 v45, v37
	v_rcp_f32_e32 v46, v38
	ds_read_b128 v[34:37], v0 offset:192
	v_rcp_f32_e32 v47, v39
	v_rcp_f32_e32 v48, v40
	v_rcp_f32_e32 v49, v41
	ds_read_b128 v[38:41], v0 offset:224
	v_mul_f32_e32 v18, v18, v42
	s_waitcnt lgkmcnt(0)
	v_rcp_f32_e32 v0, v34
	v_rcp_f32_e32 v34, v35
	v_rcp_f32_e32 v35, v36
	v_rcp_f32_e32 v36, v37
	v_rcp_f32_e32 v37, v38
	v_rcp_f32_e32 v38, v39
	v_rcp_f32_e32 v39, v40
	v_rcp_f32_e32 v40, v41
	v_bfe_u32 v41, v18, 16, 1
	v_add3_u32 v18, v18, v41, s71
	v_mul_f32_e32 v2, v2, v42
	ds_write_b16_d16_hi v176, v18
	v_bfe_u32 v18, v2, 16, 1
	v_add3_u32 v2, v2, v18, s71
	ds_write_b16_d16_hi v176, v2 offset:64
	v_mul_f32_e32 v2, v19, v43
	v_bfe_u32 v18, v2, 16, 1
	v_add3_u32 v2, v2, v18, s71
	ds_write_b16_d16_hi v176, v2 offset:128
	v_mul_f32_e32 v2, v3, v43
	v_bfe_u32 v3, v2, 16, 1
	v_add3_u32 v2, v2, v3, s71
	ds_write_b16_d16_hi v176, v2 offset:192
	v_mul_f32_e32 v2, v20, v44
	v_bfe_u32 v3, v2, 16, 1
	v_add3_u32 v2, v2, v3, s71
	ds_write_b16_d16_hi v176, v2 offset:256
	v_mul_f32_e32 v2, v4, v44
	v_bfe_u32 v3, v2, 16, 1
	v_add3_u32 v2, v2, v3, s71
	ds_write_b16_d16_hi v176, v2 offset:320
	v_mul_f32_e32 v2, v21, v45
	v_bfe_u32 v3, v2, 16, 1
	v_add3_u32 v2, v2, v3, s71
	ds_write_b16_d16_hi v176, v2 offset:384
	v_mul_f32_e32 v2, v5, v45
	v_bfe_u32 v3, v2, 16, 1
	v_add3_u32 v2, v2, v3, s71
	ds_write_b16_d16_hi v176, v2 offset:448
	v_mul_f32_e32 v2, v22, v46
	v_bfe_u32 v3, v2, 16, 1
	v_add3_u32 v2, v2, v3, s71
	ds_write_b16_d16_hi v176, v2 offset:1024
	v_mul_f32_e32 v2, v6, v46
	v_bfe_u32 v3, v2, 16, 1
	v_add3_u32 v2, v2, v3, s71
	ds_write_b16_d16_hi v176, v2 offset:1088
	v_mul_f32_e32 v2, v23, v47
	v_bfe_u32 v3, v2, 16, 1
	v_add3_u32 v2, v2, v3, s71
	ds_write_b16_d16_hi v176, v2 offset:1152
	v_mul_f32_e32 v2, v7, v47
	v_bfe_u32 v3, v2, 16, 1
	v_add3_u32 v2, v2, v3, s71
	ds_write_b16_d16_hi v176, v2 offset:1216
	v_mul_f32_e32 v2, v24, v48
	v_bfe_u32 v3, v2, 16, 1
	v_add3_u32 v2, v2, v3, s71
	ds_write_b16_d16_hi v176, v2 offset:1280
	v_mul_f32_e32 v2, v8, v48
	v_bfe_u32 v3, v2, 16, 1
	v_add3_u32 v2, v2, v3, s71
	ds_write_b16_d16_hi v176, v2 offset:1344
	v_mul_f32_e32 v2, v25, v49
	v_bfe_u32 v3, v2, 16, 1
	v_add3_u32 v2, v2, v3, s71
	ds_write_b16_d16_hi v176, v2 offset:1408
	v_mul_f32_e32 v2, v9, v49
	v_bfe_u32 v3, v2, 16, 1
	v_add3_u32 v2, v2, v3, s71
	ds_write_b16_d16_hi v176, v2 offset:1472
	v_mul_f32_e32 v2, v26, v0
	v_bfe_u32 v3, v2, 16, 1
	v_add3_u32 v2, v2, v3, s71
	v_mul_f32_e32 v0, v10, v0
	ds_write_b16_d16_hi v176, v2 offset:2048
	v_bfe_u32 v2, v0, 16, 1
	v_add3_u32 v0, v0, v2, s71
	ds_write_b16_d16_hi v176, v0 offset:2112
	v_mul_f32_e32 v0, v27, v34
	v_bfe_u32 v2, v0, 16, 1
	v_add3_u32 v0, v0, v2, s71
	ds_write_b16_d16_hi v176, v0 offset:2176
	v_mul_f32_e32 v0, v11, v34
	v_bfe_u32 v2, v0, 16, 1
	v_add3_u32 v0, v0, v2, s71
	ds_write_b16_d16_hi v176, v0 offset:2240
	v_mul_f32_e32 v0, v28, v35
	v_bfe_u32 v2, v0, 16, 1
	v_add3_u32 v0, v0, v2, s71
	ds_write_b16_d16_hi v176, v0 offset:2304
	v_mul_f32_e32 v0, v12, v35
	v_bfe_u32 v2, v0, 16, 1
	v_add3_u32 v0, v0, v2, s71
	ds_write_b16_d16_hi v176, v0 offset:2368
	v_mul_f32_e32 v0, v29, v36
	v_bfe_u32 v2, v0, 16, 1
	v_add3_u32 v0, v0, v2, s71
	ds_write_b16_d16_hi v176, v0 offset:2432
	v_mul_f32_e32 v0, v13, v36
	v_bfe_u32 v2, v0, 16, 1
	v_add3_u32 v0, v0, v2, s71
	ds_write_b16_d16_hi v176, v0 offset:2496
	v_mul_f32_e32 v0, v30, v37
	v_bfe_u32 v2, v0, 16, 1
	v_add3_u32 v0, v0, v2, s71
	ds_write_b16_d16_hi v176, v0 offset:3072
	v_mul_f32_e32 v0, v14, v37
	v_bfe_u32 v2, v0, 16, 1
	v_add3_u32 v0, v0, v2, s71
	ds_write_b16_d16_hi v176, v0 offset:3136
	v_mul_f32_e32 v0, v31, v38
	v_bfe_u32 v2, v0, 16, 1
	v_add3_u32 v0, v0, v2, s71
	ds_write_b16_d16_hi v176, v0 offset:3200
	v_mul_f32_e32 v0, v15, v38
	v_bfe_u32 v2, v0, 16, 1
	v_add3_u32 v0, v0, v2, s71
	ds_write_b16_d16_hi v176, v0 offset:3264
	v_mul_f32_e32 v0, v32, v39
	v_bfe_u32 v2, v0, 16, 1
	v_add3_u32 v0, v0, v2, s71
	ds_write_b16_d16_hi v176, v0 offset:3328
	v_mul_f32_e32 v0, v16, v39
	v_bfe_u32 v2, v0, 16, 1
	v_add3_u32 v0, v0, v2, s71
	ds_write_b16_d16_hi v176, v0 offset:3392
	v_mul_f32_e32 v0, v33, v40
	v_bfe_u32 v2, v0, 16, 1
	v_add3_u32 v0, v0, v2, s71
	ds_write_b16_d16_hi v176, v0 offset:3456
	v_mul_f32_e32 v0, v17, v40
	v_bfe_u32 v2, v0, 16, 1
	v_add3_u32 v0, v0, v2, s71
	ds_write_b16_d16_hi v176, v0 offset:3520
	s_add_u32 s0, s18, s0
	s_waitcnt lgkmcnt(0)
	s_addc_u32 s1, s19, 0
	s_lshl_b32 s8, s23, 7
	ds_read_b128 v[2:5], v177
	ds_read_b128 v[6:9], v182
	s_add_u32 s0, s0, s8
	s_addc_u32 s1, s1, 0
	v_mov_b32_e32 v159, v1
	v_lshl_add_u64 v[14:15], s[0:1], 0, v[158:159]
	v_lshl_add_u64 v[10:11], v[14:15], 0, v[148:149]
	s_waitcnt lgkmcnt(0)
	global_store_dwordx4 v[10:11], v[2:5], off offset:1024
	ds_read_b128 v[2:5], v183
	ds_read_b128 v[10:13], v184
	v_lshl_add_u64 v[16:17], v[14:15], 0, v[150:151]
	global_store_dwordx4 v[16:17], v[6:9], off offset:1024
	s_mul_i32 s20, s22, 12
	s_mul_i32 s21, s22, 24
	v_lshl_add_u64 v[6:7], v[14:15], 0, v[152:153]
	s_waitcnt lgkmcnt(0)
	global_store_dwordx4 v[6:7], v[2:5], off offset:1024
	s_mulk_i32 s22, 0x180
	s_mov_b32 s23, 0
	v_lshl_add_u64 v[2:3], v[14:15], 0, v[154:155]
	global_store_dwordx4 v[2:3], v[10:13], off offset:1024
	s_waitcnt lgkmcnt(0)
	s_waitcnt vmcnt(0) lgkmcnt(0)
	v_readlane_b32 s88, v254, 9
	v_and_b32_e32 v234, 31, v172
	v_lshrrev_b32_e32 v239, 5, v172
	v_lshlrev_b32_e32 v235, 2, v234
	v_add_u32_e32 v235, s24, v235
	v_mul_u32_u24_e32 v240, 0x1080, v239
	v_add_u32_e32 v236, v235, v240
	v_mul_u32_u24_e32 v240, 0x84, v239
	v_add_u32_e32 v235, v235, v240
	s_cmpk_gt_u32 s20, 0x7fff
	s_cbranch_scc1 .Lcv3_w2_a
	s_lshr_b32 s84, s20, 10
	s_mov_b32 s85, 0
	s_lshl_b64 s[86:87], s[84:85], 23
	s_add_u32 s86, s12, s86
	s_addc_u32 s87, s13, s87
	s_lshl_b64 s[84:85], s[84:85], 21
	s_add_u32 s84, s28, s84
	s_addc_u32 s85, s29, s85
	s_and_b32 s80, s20, 0x3c0
	s_lshl_b32 s83, s20, 5
	s_and_b32 s83, s83, 0x7e0
	s_mov_b32 s89, 13
	s_branch .Lcv3_cm_a
.Lcv3_w2_a:
	s_add_i32 s84, s20, 0xffff8000
	s_lshl_b32 s80, s84, 1
	s_and_b32 s80, s80, 0x3c0
	s_lshl_b32 s83, s84, 5
	s_and_b32 s83, s83, 0x3e0
	s_lshr_b32 s84, s84, 9
	s_mov_b32 s85, 0
	s_lshl_b64 s[86:87], s[84:85], 22
	s_add_u32 s86, s14, s86
	s_addc_u32 s87, s15, s87
	s_lshl_b64 s[84:85], s[84:85], 20
	s_add_u32 s84, s26, s84
	s_addc_u32 s85, s27, s85
	s_mov_b32 s89, 12
.Lcv3_cm_a:
	s_lshl_b32 s90, s83, 2
	s_add_u32 s86, s86, s90
	s_addc_u32 s87, s87, 0
	v_add_u32_e32 v232, s80, v239
	v_lshlrev_b32_e32 v232, s89, v232
	v_lshl_add_u32 v232, v234, 2, v232
	s_lshl_b32 s90, 2, s89
	v_or_b32_e32 v237, s83, v234
	v_lshlrev_b32_e32 v237, 10, v237
	v_and_b32_e32 v240, 32, v172
	v_add3_u32 v237, v237, v240, s80
	global_load_dword v192, v232, s[86:87]
	v_add_u32_e32 v233, s90, v232
	global_load_dword v193, v233, s[86:87]
	v_add_u32_e32 v232, s90, v233
	global_load_dword v194, v232, s[86:87]
	v_add_u32_e32 v233, s90, v232
	global_load_dword v195, v233, s[86:87]
	v_add_u32_e32 v232, s90, v233
	global_load_dword v196, v232, s[86:87]
	v_add_u32_e32 v233, s90, v232
	global_load_dword v197, v233, s[86:87]
	v_add_u32_e32 v232, s90, v233
	global_load_dword v198, v232, s[86:87]
	v_add_u32_e32 v233, s90, v232
	global_load_dword v199, v233, s[86:87]
	v_add_u32_e32 v232, s90, v233
	global_load_dword v200, v232, s[86:87]
	v_add_u32_e32 v233, s90, v232
	global_load_dword v201, v233, s[86:87]
	v_add_u32_e32 v232, s90, v233
	global_load_dword v202, v232, s[86:87]
	v_add_u32_e32 v233, s90, v232
	global_load_dword v203, v233, s[86:87]
	v_add_u32_e32 v232, s90, v233
	global_load_dword v204, v232, s[86:87]
	v_add_u32_e32 v233, s90, v232
	global_load_dword v205, v233, s[86:87]
	v_add_u32_e32 v232, s90, v233
	global_load_dword v206, v232, s[86:87]
	v_add_u32_e32 v233, s90, v232
	global_load_dword v207, v233, s[86:87]
	v_add_u32_e32 v232, s90, v233
	global_load_dword v208, v232, s[86:87]
	v_add_u32_e32 v233, s90, v232
	global_load_dword v209, v233, s[86:87]
	v_add_u32_e32 v232, s90, v233
	global_load_dword v210, v232, s[86:87]
	v_add_u32_e32 v233, s90, v232
	global_load_dword v211, v233, s[86:87]
	v_add_u32_e32 v232, s90, v233
	global_load_dword v212, v232, s[86:87]
	v_add_u32_e32 v233, s90, v232
	global_load_dword v213, v233, s[86:87]
	v_add_u32_e32 v232, s90, v233
	global_load_dword v214, v232, s[86:87]
	v_add_u32_e32 v233, s90, v232
	global_load_dword v215, v233, s[86:87]
	v_add_u32_e32 v232, s90, v233
	global_load_dword v216, v232, s[86:87]
	v_add_u32_e32 v233, s90, v232
	global_load_dword v217, v233, s[86:87]
	v_add_u32_e32 v232, s90, v233
	global_load_dword v218, v232, s[86:87]
	v_add_u32_e32 v233, s90, v232
	global_load_dword v219, v233, s[86:87]
	v_add_u32_e32 v232, s90, v233
	global_load_dword v220, v232, s[86:87]
	v_add_u32_e32 v233, s90, v232
	global_load_dword v221, v233, s[86:87]
	v_add_u32_e32 v232, s90, v233
	global_load_dword v222, v232, s[86:87]
	v_add_u32_e32 v233, s90, v232
	global_load_dword v223, v233, s[86:87]
	s_waitcnt vmcnt(0)
	s_branch .Lcv3_body

.Lcv3_body:
	v_mul_f32_e32 v8, 0x42800000, v192
	v_mul_f32_e32 v9, 0x42800000, v193
	v_mul_f32_e32 v10, 0x42800000, v194
	v_mul_f32_e32 v11, 0x42800000, v195
	v_mul_f32_e32 v12, 0x42800000, v196
	v_mul_f32_e32 v13, 0x42800000, v197
	v_mul_f32_e32 v14, 0x42800000, v198
	v_mul_f32_e32 v15, 0x42800000, v199
	v_mul_f32_e32 v16, 0x42800000, v200
	v_mul_f32_e32 v17, 0x42800000, v201
	v_mul_f32_e32 v18, 0x42800000, v202
	v_mul_f32_e32 v19, 0x42800000, v203
	v_mul_f32_e32 v20, 0x42800000, v204
	v_mul_f32_e32 v21, 0x42800000, v205
	v_mul_f32_e32 v22, 0x42800000, v206
	v_mul_f32_e32 v23, 0x42800000, v207
	v_mul_f32_e32 v24, 0x42800000, v208
	v_mul_f32_e32 v25, 0x42800000, v209
	v_mul_f32_e32 v26, 0x42800000, v210
	v_mul_f32_e32 v27, 0x42800000, v211
	v_mul_f32_e32 v28, 0x42800000, v212
	v_mul_f32_e32 v29, 0x42800000, v213
	v_mul_f32_e32 v30, 0x42800000, v214
	v_mul_f32_e32 v31, 0x42800000, v215
	v_mul_f32_e32 v32, 0x42800000, v216
	v_mul_f32_e32 v33, 0x42800000, v217
	v_mul_f32_e32 v34, 0x42800000, v218
	v_mul_f32_e32 v35, 0x42800000, v219
	v_mul_f32_e32 v36, 0x42800000, v220
	v_mul_f32_e32 v37, 0x42800000, v221
	v_mul_f32_e32 v38, 0x42800000, v222
	v_mul_f32_e32 v39, 0x42800000, v223
	s_mov_b64 s[98:99], s[84:85]
	v_mov_b32_e32 v238, v237
	s_add_i32 s20, s20, 1
	s_add_i32 s23, s23, 2
	s_cmp_eq_u32 s23, 24
	s_cbranch_scc1 .Lcv3_noissue
	s_cmpk_gt_u32 s20, 0x7fff
	s_cbranch_scc1 .Lcv3_w2_b
	s_lshr_b32 s84, s20, 10
	s_mov_b32 s85, 0
	s_lshl_b64 s[86:87], s[84:85], 23
	s_add_u32 s86, s12, s86
	s_addc_u32 s87, s13, s87
	s_lshl_b64 s[84:85], s[84:85], 21
	s_add_u32 s84, s28, s84
	s_addc_u32 s85, s29, s85
	s_and_b32 s80, s20, 0x3c0
	s_lshl_b32 s83, s20, 5
	s_and_b32 s83, s83, 0x7e0
	s_mov_b32 s89, 13
	s_branch .Lcv3_cm_b

.Lcv3_cm_b:
	s_lshl_b32 s90, s83, 2
	s_add_u32 s86, s86, s90
	s_addc_u32 s87, s87, 0
	v_add_u32_e32 v232, s80, v239
	v_lshlrev_b32_e32 v232, s89, v232
	v_lshl_add_u32 v232, v234, 2, v232
	s_lshl_b32 s90, 2, s89
	v_or_b32_e32 v237, s83, v234
	v_lshlrev_b32_e32 v237, 10, v237
	v_and_b32_e32 v240, 32, v172
	v_add3_u32 v237, v237, v240, s80
	global_load_dword v192, v232, s[86:87]
	v_add_u32_e32 v233, s90, v232
	global_load_dword v193, v233, s[86:87]
	v_add_u32_e32 v232, s90, v233
	global_load_dword v194, v232, s[86:87]
	v_add_u32_e32 v233, s90, v232
	global_load_dword v195, v233, s[86:87]
	v_add_u32_e32 v232, s90, v233
	global_load_dword v196, v232, s[86:87]
	v_add_u32_e32 v233, s90, v232
	global_load_dword v197, v233, s[86:87]
	v_add_u32_e32 v232, s90, v233
	global_load_dword v198, v232, s[86:87]
	v_add_u32_e32 v233, s90, v232
	global_load_dword v199, v233, s[86:87]
	v_add_u32_e32 v232, s90, v233
	global_load_dword v200, v232, s[86:87]
	v_add_u32_e32 v233, s90, v232
	global_load_dword v201, v233, s[86:87]
	v_add_u32_e32 v232, s90, v233
	global_load_dword v202, v232, s[86:87]
	v_add_u32_e32 v233, s90, v232
	global_load_dword v203, v233, s[86:87]
	v_add_u32_e32 v232, s90, v233
	global_load_dword v204, v232, s[86:87]
	v_add_u32_e32 v233, s90, v232
	global_load_dword v205, v233, s[86:87]
	v_add_u32_e32 v232, s90, v233
	global_load_dword v206, v232, s[86:87]
	v_add_u32_e32 v233, s90, v232
	global_load_dword v207, v233, s[86:87]
	v_add_u32_e32 v232, s90, v233
	global_load_dword v208, v232, s[86:87]
	v_add_u32_e32 v233, s90, v232
	global_load_dword v209, v233, s[86:87]
	v_add_u32_e32 v232, s90, v233
	global_load_dword v210, v232, s[86:87]
	v_add_u32_e32 v233, s90, v232
	global_load_dword v211, v233, s[86:87]
	v_add_u32_e32 v232, s90, v233
	global_load_dword v212, v232, s[86:87]
	v_add_u32_e32 v233, s90, v232
	global_load_dword v213, v233, s[86:87]
	v_add_u32_e32 v232, s90, v233
	global_load_dword v214, v232, s[86:87]
	v_add_u32_e32 v233, s90, v232
	global_load_dword v215, v233, s[86:87]
	v_add_u32_e32 v232, s90, v233
	global_load_dword v216, v232, s[86:87]
	v_add_u32_e32 v233, s90, v232
	global_load_dword v217, v233, s[86:87]
	v_add_u32_e32 v232, s90, v233
	global_load_dword v218, v232, s[86:87]
	v_add_u32_e32 v233, s90, v232
	global_load_dword v219, v233, s[86:87]
	v_add_u32_e32 v232, s90, v233
	global_load_dword v220, v232, s[86:87]
	v_add_u32_e32 v233, s90, v232
	global_load_dword v221, v233, s[86:87]
	v_add_u32_e32 v232, s90, v233
	global_load_dword v222, v232, s[86:87]
	v_add_u32_e32 v233, s90, v232
	global_load_dword v223, v233, s[86:87]
.Lcv3_noissue:
	ds_write2_b32 v235, v8, v9 offset0:0 offset1:66
	ds_write2_b32 v235, v10, v11 offset0:132 offset1:198
	v_add_u32_e32 v240, 0x400, v235
	ds_write2_b32 v240, v12, v13 offset0:8 offset1:74
	ds_write2_b32 v240, v14, v15 offset0:140 offset1:206
	v_add_u32_e32 v240, 0x800, v235
	ds_write2_b32 v240, v16, v17 offset0:16 offset1:82
	ds_write2_b32 v240, v18, v19 offset0:148 offset1:214
	v_add_u32_e32 v240, 0xc00, v235
	ds_write2_b32 v240, v20, v21 offset0:24 offset1:90
	ds_write2_b32 v240, v22, v23 offset0:156 offset1:222
	v_add_u32_e32 v240, 0x1000, v235
	ds_write2_b32 v240, v24, v25 offset0:32 offset1:98
	ds_write2_b32 v240, v26, v27 offset0:164 offset1:230
	v_add_u32_e32 v240, 0x1400, v235
	ds_write2_b32 v240, v28, v29 offset0:40 offset1:106
	ds_write2_b32 v240, v30, v31 offset0:172 offset1:238
	v_add_u32_e32 v240, 0x1800, v235
	ds_write2_b32 v240, v32, v33 offset0:48 offset1:114
	ds_write2_b32 v240, v34, v35 offset0:180 offset1:246
	v_add_u32_e32 v240, 0x1c00, v235
	ds_write2_b32 v240, v36, v37 offset0:56 offset1:122
	ds_write2_b32 v240, v38, v39 offset0:188 offset1:254
	s_waitcnt lgkmcnt(0)
	ds_read2_b32 v[8:9], v236 offset0:0 offset1:33
	ds_read2_b32 v[10:11], v236 offset0:66 offset1:99
	ds_read2_b32 v[12:13], v236 offset0:132 offset1:165
	ds_read2_b32 v[14:15], v236 offset0:198 offset1:231
	v_add_u32_e32 v240, 0x400, v236
	ds_read2_b32 v[16:17], v240 offset0:8 offset1:41
	ds_read2_b32 v[18:19], v240 offset0:74 offset1:107
	ds_read2_b32 v[20:21], v240 offset0:140 offset1:173
	ds_read2_b32 v[22:23], v240 offset0:206 offset1:239
	v_add_u32_e32 v240, 0x800, v236
	ds_read2_b32 v[24:25], v240 offset0:16 offset1:49
	ds_read2_b32 v[26:27], v240 offset0:82 offset1:115
	ds_read2_b32 v[28:29], v240 offset0:148 offset1:181
	ds_read2_b32 v[30:31], v240 offset0:214 offset1:247
	v_add_u32_e32 v240, 0xc00, v236
	ds_read2_b32 v[32:33], v240 offset0:24 offset1:57
	ds_read2_b32 v[34:35], v240 offset0:90 offset1:123
	ds_read2_b32 v[36:37], v240 offset0:156 offset1:189
	ds_read2_b32 v[38:39], v240 offset0:222 offset1:255
	s_waitcnt lgkmcnt(14)
	v_med3_f32 v8, v8, s73, v188
	v_med3_f32 v9, v9, s73, v188
	v_med3_f32 v10, v10, s73, v188
	v_med3_f32 v11, v11, s73, v188
	v_cvt_pk_fp8_f32 v224, v8, v9
	v_cvt_pk_fp8_f32 v224, v10, v11 op_sel:[0,0,1]
	s_waitcnt lgkmcnt(12)
	v_med3_f32 v12, v12, s73, v188
	v_med3_f32 v13, v13, s73, v188
	v_med3_f32 v14, v14, s73, v188
	v_med3_f32 v15, v15, s73, v188
	v_cvt_pk_fp8_f32 v225, v12, v13
	v_cvt_pk_fp8_f32 v225, v14, v15 op_sel:[0,0,1]
	s_waitcnt lgkmcnt(10)
	v_med3_f32 v16, v16, s73, v188
	v_med3_f32 v17, v17, s73, v188
	v_med3_f32 v18, v18, s73, v188
	v_med3_f32 v19, v19, s73, v188
	v_cvt_pk_fp8_f32 v226, v16, v17
	v_cvt_pk_fp8_f32 v226, v18, v19 op_sel:[0,0,1]
	s_waitcnt lgkmcnt(8)
	v_med3_f32 v20, v20, s73, v188
	v_med3_f32 v21, v21, s73, v188
	v_med3_f32 v22, v22, s73, v188
	v_med3_f32 v23, v23, s73, v188
	v_cvt_pk_fp8_f32 v227, v20, v21
	v_cvt_pk_fp8_f32 v227, v22, v23 op_sel:[0,0,1]
	s_waitcnt lgkmcnt(6)
	v_med3_f32 v24, v24, s73, v188
	v_med3_f32 v25, v25, s73, v188
	v_med3_f32 v26, v26, s73, v188
	v_med3_f32 v27, v27, s73, v188
	v_cvt_pk_fp8_f32 v228, v24, v25
	v_cvt_pk_fp8_f32 v228, v26, v27 op_sel:[0,0,1]
	s_waitcnt lgkmcnt(4)
	v_med3_f32 v28, v28, s73, v188
	v_med3_f32 v29, v29, s73, v188
	v_med3_f32 v30, v30, s73, v188
	v_med3_f32 v31, v31, s73, v188
	v_cvt_pk_fp8_f32 v229, v28, v29
	v_cvt_pk_fp8_f32 v229, v30, v31 op_sel:[0,0,1]
	s_waitcnt lgkmcnt(2)
	v_med3_f32 v32, v32, s73, v188
	v_med3_f32 v33, v33, s73, v188
	v_med3_f32 v34, v34, s73, v188
	v_med3_f32 v35, v35, s73, v188
	v_cvt_pk_fp8_f32 v230, v32, v33
	v_cvt_pk_fp8_f32 v230, v34, v35 op_sel:[0,0,1]
	s_waitcnt lgkmcnt(0)
	v_med3_f32 v36, v36, s73, v188
	v_med3_f32 v37, v37, s73, v188
	v_med3_f32 v38, v38, s73, v188
	v_med3_f32 v39, v39, s73, v188
	v_cvt_pk_fp8_f32 v231, v36, v37
	v_cvt_pk_fp8_f32 v231, v38, v39 op_sel:[0,0,1]
	global_store_dwordx4 v238, v[224:227], s[98:99]
	global_store_dwordx4 v238, v[228:231], s[98:99] offset:16
	s_cmp_eq_u32 s23, 24
	s_cbranch_scc0 .Lcv3_top
	s_branch .LBB0_322
